# speedup vs baseline: 1.0056x; 1.0051x over previous
_Z6k_normPKfP15HIP_vector_typeIjLj4EEPfPyS4_:
	s_load_dwordx2 s[4:5], s[0:1], 0x0
	s_ashr_i32 s3, s2, 31
	s_lshl_b64 s[6:7], s[2:3], 16
	v_and_b32_e32 v1, 63, v0
	s_waitcnt lgkmcnt(0)
	s_add_u32 s4, s4, s6
	v_lshrrev_b32_e32 v66, 6, v0
	s_addc_u32 s5, s5, s7
	v_lshlrev_b32_e32 v2, 4, v1
	v_mov_b32_e32 v3, 0
	v_lshl_add_u64 v[4:5], s[4:5], 0, v[2:3]
	v_lshlrev_b32_e32 v2, 14, v66
	v_lshl_add_u64 v[2:3], v[4:5], 0, v[2:3]
	s_movk_i32 s3, 0x1000
	v_add_co_u32_e32 v68, vcc, s3, v2
	s_movk_i32 s3, 0x2000
	s_nop 0
	v_addc_co_u32_e32 v69, vcc, 0, v3, vcc
	v_add_co_u32_e32 v70, vcc, s3, v2
	s_nop 1
	v_addc_co_u32_e32 v71, vcc, 0, v3, vcc
	v_add_co_u32_e32 v72, vcc, 0x3000, v2
	s_nop 1
	v_addc_co_u32_e32 v73, vcc, 0, v3, vcc
	global_load_dwordx4 v[62:65], v[2:3], off nt
	global_load_dwordx4 v[58:61], v[2:3], off offset:1024 nt
	global_load_dwordx4 v[50:53], v[2:3], off offset:2048 nt
	global_load_dwordx4 v[46:49], v[2:3], off offset:3072 nt
	global_load_dwordx4 v[54:57], v[70:71], off offset:-4096 nt
	global_load_dwordx4 v[42:45], v[68:69], off offset:1024 nt
	global_load_dwordx4 v[34:37], v[68:69], off offset:2048 nt
	global_load_dwordx4 v[38:41], v[68:69], off offset:3072 nt
	global_load_dwordx4 v[30:33], v[70:71], off nt
	global_load_dwordx4 v[26:29], v[70:71], off offset:1024 nt
	global_load_dwordx4 v[22:25], v[70:71], off offset:2048 nt
	global_load_dwordx4 v[18:21], v[70:71], off offset:3072 nt
	global_load_dwordx4 v[14:17], v[72:73], off nt
	global_load_dwordx4 v[10:13], v[72:73], off offset:1024 nt
	global_load_dwordx4 v[6:9], v[72:73], off offset:2048 nt
	global_load_dwordx4 v[2:5], v[72:73], off offset:3072 nt
	v_cmp_gt_u32_e32 vcc, 32, v0
	s_and_saveexec_b64 s[6:7], vcc
	s_cbranch_execz .LBB0_2
	s_load_dwordx2 s[8:9], s[0:1], 0x18
	v_lshl_or_b32 v84, s2, 5, v0
	v_mov_b32_e32 v86, 0
	v_ashrrev_i32_e32 v85, 31, v84
	v_mov_b32_e32 v87, v86
	s_waitcnt lgkmcnt(0)
	v_lshl_add_u64 v[84:85], v[84:85], 3, s[8:9]
	global_store_dwordx2 v[84:85], v[86:87], off

.LBB0_4:
	s_or_b64 exec, exec, s[6:7]
	v_lshrrev_b32_e32 v87, 1, v1
	v_lshrrev_b32_e32 v88, 6, v0
	v_lshlrev_b32_e32 v88, 3, v88
	v_xor_b32_e32 v88, v88, v87
	v_lshlrev_b32_e32 v88, 4, v88
	v_lshl_or_b32 v87, v87, 9, v88
	v_and_b32_e32 v88, 1, v1
	v_lshl_or_b32 v87, v88, 3, v87
	v_lshrrev_b32_e32 v88, 5, v0
	v_and_b32_e32 v89, 31, v0
	v_xor_b32_e32 v89, v89, v88
	v_lshlrev_b32_e32 v89, 4, v89
	v_lshl_or_b32 v88, v88, 9, v89
	v_lshlrev_b32_e32 v89, 4, v0
	s_waitcnt vmcnt(14)
	v_mul_f32_e32 v67, v63, v63
	v_fmac_f32_e32 v67, v62, v62
	v_fmac_f32_e32 v67, v64, v64
	v_fmac_f32_e32 v67, v65, v65
	v_fmac_f32_e32 v67, v58, v58
	v_fmac_f32_e32 v67, v59, v59
	v_fmac_f32_e32 v67, v60, v60
	v_fmac_f32_e32 v67, v61, v61
	v_add_f32_e32 v75, v62, v63
	v_add_f32_e32 v83, v64, v65
	v_add_f32_e32 v75, v75, v83
	v_add_f32_e32 v84, v58, v59
	v_add_f32_e32 v85, v60, v61
	v_add_f32_e32 v84, v84, v85
	v_add_f32_e32 v75, v75, v84
	s_waitcnt vmcnt(12)
	v_mul_f32_e32 v68, v51, v51
	v_fmac_f32_e32 v68, v50, v50
	v_fmac_f32_e32 v68, v52, v52
	v_fmac_f32_e32 v68, v53, v53
	v_fmac_f32_e32 v68, v46, v46
	v_fmac_f32_e32 v68, v47, v47
	v_fmac_f32_e32 v68, v48, v48
	v_fmac_f32_e32 v68, v49, v49
	v_add_f32_e32 v76, v50, v51
	v_add_f32_e32 v83, v52, v53
	v_add_f32_e32 v76, v76, v83
	v_add_f32_e32 v84, v46, v47
	v_add_f32_e32 v85, v48, v49
	v_add_f32_e32 v84, v84, v85
	v_add_f32_e32 v76, v76, v84
	s_waitcnt vmcnt(10)
	v_mul_f32_e32 v69, v55, v55
	v_fmac_f32_e32 v69, v54, v54
	v_fmac_f32_e32 v69, v56, v56
	v_fmac_f32_e32 v69, v57, v57
	v_fmac_f32_e32 v69, v42, v42
	v_fmac_f32_e32 v69, v43, v43
	v_fmac_f32_e32 v69, v44, v44
	v_fmac_f32_e32 v69, v45, v45
	v_add_f32_e32 v77, v54, v55
	v_add_f32_e32 v83, v56, v57
	v_add_f32_e32 v77, v77, v83
	v_add_f32_e32 v84, v42, v43
	v_add_f32_e32 v85, v44, v45
	v_add_f32_e32 v84, v84, v85
	v_add_f32_e32 v77, v77, v84
	s_waitcnt vmcnt(8)
	v_mul_f32_e32 v70, v35, v35
	v_fmac_f32_e32 v70, v34, v34
	v_fmac_f32_e32 v70, v36, v36
	v_fmac_f32_e32 v70, v37, v37
	v_fmac_f32_e32 v70, v38, v38
	v_fmac_f32_e32 v70, v39, v39
	v_fmac_f32_e32 v70, v40, v40
	v_fmac_f32_e32 v70, v41, v41
	v_add_f32_e32 v78, v34, v35
	v_add_f32_e32 v83, v36, v37
	v_add_f32_e32 v78, v78, v83
	v_add_f32_e32 v84, v38, v39
	v_add_f32_e32 v85, v40, v41
	v_add_f32_e32 v84, v84, v85
	v_add_f32_e32 v78, v78, v84
	s_waitcnt vmcnt(6)
	v_mul_f32_e32 v71, v31, v31
	v_fmac_f32_e32 v71, v30, v30
	v_fmac_f32_e32 v71, v32, v32
	v_fmac_f32_e32 v71, v33, v33
	v_fmac_f32_e32 v71, v26, v26
	v_fmac_f32_e32 v71, v27, v27
	v_fmac_f32_e32 v71, v28, v28
	v_fmac_f32_e32 v71, v29, v29
	v_add_f32_e32 v79, v30, v31
	v_add_f32_e32 v83, v32, v33
	v_add_f32_e32 v79, v79, v83
	v_add_f32_e32 v84, v26, v27
	v_add_f32_e32 v85, v28, v29
	v_add_f32_e32 v84, v84, v85
	v_add_f32_e32 v79, v79, v84
	s_waitcnt vmcnt(4)
	v_mul_f32_e32 v72, v23, v23
	v_fmac_f32_e32 v72, v22, v22
	v_fmac_f32_e32 v72, v24, v24
	v_fmac_f32_e32 v72, v25, v25
	v_fmac_f32_e32 v72, v18, v18
	v_fmac_f32_e32 v72, v19, v19
	v_fmac_f32_e32 v72, v20, v20
	v_fmac_f32_e32 v72, v21, v21
	v_add_f32_e32 v80, v22, v23
	v_add_f32_e32 v83, v24, v25
	v_add_f32_e32 v80, v80, v83
	v_add_f32_e32 v84, v18, v19
	v_add_f32_e32 v85, v20, v21
	v_add_f32_e32 v84, v84, v85
	v_add_f32_e32 v80, v80, v84
	s_waitcnt vmcnt(2)
	v_mul_f32_e32 v73, v15, v15
	v_fmac_f32_e32 v73, v14, v14
	v_fmac_f32_e32 v73, v16, v16
	v_fmac_f32_e32 v73, v17, v17
	v_fmac_f32_e32 v73, v10, v10
	v_fmac_f32_e32 v73, v11, v11
	v_fmac_f32_e32 v73, v12, v12
	v_fmac_f32_e32 v73, v13, v13
	v_add_f32_e32 v81, v14, v15
	v_add_f32_e32 v83, v16, v17
	v_add_f32_e32 v81, v81, v83
	v_add_f32_e32 v84, v10, v11
	v_add_f32_e32 v85, v12, v13
	v_add_f32_e32 v84, v84, v85
	v_add_f32_e32 v81, v81, v84
	s_waitcnt vmcnt(0)
	v_mul_f32_e32 v74, v7, v7
	v_fmac_f32_e32 v74, v6, v6
	v_fmac_f32_e32 v74, v8, v8
	v_fmac_f32_e32 v74, v9, v9
	v_fmac_f32_e32 v74, v2, v2
	v_fmac_f32_e32 v74, v3, v3
	v_fmac_f32_e32 v74, v4, v4
	v_fmac_f32_e32 v74, v5, v5
	v_add_f32_e32 v82, v6, v7
	v_add_f32_e32 v83, v8, v9
	v_add_f32_e32 v82, v82, v83
	v_add_f32_e32 v84, v2, v3
	v_add_f32_e32 v85, v4, v5
	v_add_f32_e32 v84, v84, v85
	v_add_f32_e32 v82, v82, v84
	v_and_b32_e32 v83, 8, v0
	v_cmp_ne_u32_e64 s[6:7], 0, v83
	v_permlane32_swap_b32_e32 v67, v71
	v_permlane32_swap_b32_e32 v75, v79
	v_permlane32_swap_b32_e32 v68, v72
	v_permlane32_swap_b32_e32 v76, v80
	v_permlane32_swap_b32_e32 v69, v73
	v_permlane32_swap_b32_e32 v77, v81
	v_permlane32_swap_b32_e32 v70, v74
	v_permlane32_swap_b32_e32 v78, v82
	v_add_f32_e32 v67, v67, v71
	v_add_f32_e32 v75, v75, v79
	v_add_f32_e32 v68, v68, v72
	v_add_f32_e32 v76, v76, v80
	v_add_f32_e32 v69, v69, v73
	v_add_f32_e32 v77, v77, v81
	v_add_f32_e32 v70, v70, v74
	v_add_f32_e32 v78, v78, v82
	s_nop 1
	v_permlane16_swap_b32_e32 v67, v69
	v_permlane16_swap_b32_e32 v75, v77
	v_permlane16_swap_b32_e32 v68, v70
	v_permlane16_swap_b32_e32 v76, v78
	v_add_f32_e32 v67, v67, v69
	v_add_f32_e32 v75, v75, v77
	v_add_f32_e32 v68, v68, v70
	v_add_f32_e32 v76, v76, v78
	v_cndmask_b32_e64 v83, v67, v68, s[6:7]
	v_cndmask_b32_e64 v84, v68, v67, s[6:7]
	v_cndmask_b32_e64 v85, v75, v76, s[6:7]
	v_cndmask_b32_e64 v86, v76, v75, s[6:7]
	s_nop 1
	v_add_f32_dpp v67, v84, v83 row_ror:8 row_mask:0xf bank_mask:0xf
	v_add_f32_dpp v69, v86, v85 row_ror:8 row_mask:0xf bank_mask:0xf
	s_nop 1
	v_add_f32_dpp v67, v67, v67 row_half_mirror row_mask:0xf bank_mask:0xf
	v_add_f32_dpp v69, v69, v69 row_half_mirror row_mask:0xf bank_mask:0xf
	s_nop 1
	v_add_f32_dpp v67, v67, v67 quad_perm:[2,3,0,1] row_mask:0xf bank_mask:0xf
	v_add_f32_dpp v69, v69, v69 quad_perm:[2,3,0,1] row_mask:0xf bank_mask:0xf
	s_nop 1
	v_add_f32_dpp v67, v67, v67 quad_perm:[1,0,3,2] row_mask:0xf bank_mask:0xf
	v_add_f32_dpp v69, v69, v69 quad_perm:[1,0,3,2] row_mask:0xf bank_mask:0xf
	s_mov_b32 s3, 0xf800000
	v_mul_f32_e32 v70, 0x4f800000, v67
	v_cmp_gt_f32_e32 vcc, s3, v67
	s_nop 1
	v_cndmask_b32_e32 v67, v67, v70, vcc
	v_sqrt_f32_e32 v70, v67
	s_nop 0
	v_add_u32_e32 v68, -1, v70
	v_fma_f32 v73, -v68, v70, v67
	v_cmp_ge_f32_e64 s[4:5], 0, v73
	v_add_u32_e32 v73, 1, v70
	s_nop 0
	v_cndmask_b32_e64 v68, v70, v68, s[4:5]
	v_fma_f32 v70, -v73, v70, v67
	v_cmp_lt_f32_e64 s[4:5], 0, v70
	s_nop 1
	v_cndmask_b32_e64 v68, v68, v73, s[4:5]
	v_mul_f32_e32 v70, 0x37800000, v68
	v_cndmask_b32_e32 v68, v68, v70, vcc
	v_mov_b32_e32 v70, 0x260
	v_cmp_class_f32_e32 vcc, v67, v70
	s_nop 1
	v_cndmask_b32_e32 v67, v68, v67, vcc
	v_max_f32_e32 v68, 0x322bcc77, v67
	v_div_scale_f32 v67, s[4:5], v68, v68, 1.0
	v_rcp_f32_e32 v73, v67
	s_load_dwordx2 s[4:5], s[0:1], 0x8
	v_fma_f32 v71, -v67, v73, 1.0
	v_fmac_f32_e32 v73, v71, v73
	v_div_scale_f32 v71, vcc, 1.0, v68, 1.0
	v_mul_f32_e32 v72, v71, v73
	v_fma_f32 v74, -v67, v72, v71
	v_fmac_f32_e32 v72, v74, v73
	v_fma_f32 v67, -v67, v72, v71
	v_div_fmas_f32 v71, v67, v73, v72
	v_mov_b32_e32 v70, 0
	v_and_b32_e32 v67, 7, v0
	v_cmp_ne_u32_e32 vcc, 0, v67
	v_lshlrev_b32_e32 v67, 3, v66
	s_and_saveexec_b64 s[6:7], vcc
	s_xor_b64 s[6:7], exec, s[6:7]
	v_lshlrev_b32_e32 v67, 3, v66
	s_or_saveexec_b64 s[6:7], s[6:7]
	v_div_fixup_f32 v66, v71, v68, 1.0
	s_xor_b64 exec, exec, s[6:7]
	s_cbranch_execz .LBB0_10
	s_load_dwordx2 s[0:1], s[0:1], 0x10
	s_waitcnt lgkmcnt(0)
	v_add_f32_e32 v68, v69, v70
	v_mul_f32_e32 v70, v68, v66
	s_lshl_b32 s3, s2, 5
	v_lshrrev_b32_e32 v68, 3, v1
	v_or3_b32 v68, v67, s3, v68
	v_ashrrev_i32_e32 v69, 31, v68
	v_lshl_add_u64 v[68:69], v[68:69], 2, s[0:1]
	global_store_dword v[68:69], v70, off
